# loader waves stage tile i+2 at the end of iteration i behind a counted lgkmcnt(4); iterations start with the B-fragment reads
# baseline (speedup 1.0000x reference)
.LBB0_82:
	s_waitcnt vmcnt(3)
	v_cvt_pk_f16_f32 v67, v168, v169
	v_cvt_pk_f16_f32 v66, v166, v167
	ds_write_b64 v192, v[66:67]
	s_waitcnt vmcnt(2)
	v_cvt_pk_f16_f32 v67, v164, v165
	v_cvt_pk_f16_f32 v66, v162, v163
	ds_write_b64 v192, v[66:67] offset:2304
	s_add_i32 s6, s0, -1
	s_add_i32 s5, s0, -2
	s_and_b32 s6, s6, 3
	s_min_u32 s7, s5, 12
	s_lshl_b32 s6, s6, 13
	v_lshl_add_u32 v66, s7, 13, v190
	s_add_i32 s6, s6, 0x12000
	v_or_b32_e32 v66, v66, v178
	v_lshl_or_b32 v67, v187, 4, s6
	v_lshl_or_b32 v84, v188, 4, s6
	v_or_b32_e32 v85, 0x1000, v66
	ds_write_b128 v67, v[166:169]
	ds_write_b128 v84, v[162:165]
	global_load_dwordx4 v[166:169], v66, s[20:21] nt
	global_load_dwordx4 v[162:165], v85, s[20:21] nt
.Lld_even:
	s_add_i32 s5, s0, -2
	ds_read_b128 v[194:197], v193
	ds_read_b128 v[198:201], v193 offset:32
	ds_read_b128 v[202:205], v193 offset:64
	ds_read_b128 v[206:209], v193 offset:96
	s_waitcnt lgkmcnt(3)
	v_mfma_f32_32x32x16_f16 v[66:81], v[98:101], v[194:197], v[2:17]
	s_waitcnt lgkmcnt(2)
	v_mfma_f32_32x32x16_f16 v[66:81], v[102:105], v[198:201], v[66:81]
	s_waitcnt lgkmcnt(1)
	v_mfma_f32_32x32x16_f16 v[66:81], v[106:109], v[202:205], v[66:81]
	s_waitcnt lgkmcnt(0)
	v_mfma_f32_32x32x16_f16 v[66:81], v[110:113], v[206:209], v[66:81]
	v_mfma_f32_32x32x16_f16 v[82:97], v[114:117], v[194:197], v[18:33]
	s_nop 10
	v_and_b32_e32 v66, 0xffffffc0, v66
	v_and_or_b32 v67, v67, s1, 1
	v_and_or_b32 v68, v68, s1, 2
	v_and_or_b32 v69, v69, s1, 3
	v_med3_f32 v211, v66, v67, s4
	v_and_or_b32 v70, v70, s1, 4
	v_min3_f32 v210, v66, s4, v67
	v_and_or_b32 v71, v71, s1, 5
	v_mfma_f32_32x32x16_f16 v[82:97], v[118:121], v[198:201], v[82:97]
	v_med3_f32 v214, v210, v68, v69
	v_and_or_b32 v72, v72, s1, 6
	v_min3_f32 v212, v210, v68, v69
	v_and_or_b32 v73, v73, s1, 7
	v_min3_f32 v213, v211, s4, v214
	v_med3_f32 v211, v212, v70, v71
	v_and_or_b32 v74, v74, s1, 8
	v_min3_f32 v210, v212, v70, v71
	v_mfma_f32_32x32x16_f16 v[82:97], v[122:125], v[202:205], v[82:97]
	v_and_or_b32 v75, v75, s1, 9
	v_med3_f32 v214, v210, v72, v73
	v_and_or_b32 v76, v76, s1, 10
	v_min3_f32 v212, v210, v72, v73
	v_and_or_b32 v77, v77, s1, 11
	v_min3_f32 v213, v213, v211, v214
	v_med3_f32 v211, v212, v74, v75
	v_and_or_b32 v78, v78, s1, 12
	v_mfma_f32_32x32x16_f16 v[82:97], v[126:129], v[206:209], v[82:97]
	v_min3_f32 v210, v212, v74, v75
	v_and_or_b32 v79, v79, s1, 13
	v_med3_f32 v214, v210, v76, v77
	v_and_or_b32 v80, v80, s1, 14
	v_min3_f32 v212, v210, v76, v77
	v_and_or_b32 v81, v81, s1, 15
	v_min3_f32 v213, v213, v211, v214
	v_med3_f32 v211, v212, v78, v79
	v_min3_f32 v210, v212, v78, v79
	v_med3_f32 v214, v210, v80, v81
	v_min3_f32 v212, v210, v80, v81
	v_min3_f32 v213, v213, v211, v214
	v_mfma_f32_32x32x16_f16 v[66:81], v[130:133], v[194:197], v[34:49]
	v_and_or_b32 v82, v82, s1, 16
	v_and_or_b32 v83, v83, s1, 17
	v_and_or_b32 v84, v84, s1, 18
	v_and_or_b32 v85, v85, s1, 19
	v_med3_f32 v211, v212, v82, v83
	v_and_or_b32 v86, v86, s1, 20
	v_min3_f32 v210, v212, v82, v83
	v_and_or_b32 v87, v87, s1, 21
	v_mfma_f32_32x32x16_f16 v[66:81], v[134:137], v[198:201], v[66:81]
	v_med3_f32 v214, v210, v84, v85
	v_and_or_b32 v88, v88, s1, 22
	v_min3_f32 v212, v210, v84, v85
	v_and_or_b32 v89, v89, s1, 23
	v_min3_f32 v213, v213, v211, v214
	v_med3_f32 v211, v212, v86, v87
	v_and_or_b32 v90, v90, s1, 24
	v_min3_f32 v210, v212, v86, v87
	v_mfma_f32_32x32x16_f16 v[66:81], v[138:141], v[202:205], v[66:81]
	v_and_or_b32 v91, v91, s1, 25
	v_med3_f32 v214, v210, v88, v89
	v_and_or_b32 v92, v92, s1, 26
	v_min3_f32 v212, v210, v88, v89
	v_and_or_b32 v93, v93, s1, 27
	v_min3_f32 v213, v213, v211, v214
	v_med3_f32 v211, v212, v90, v91
	v_and_or_b32 v94, v94, s1, 28
	v_mfma_f32_32x32x16_f16 v[66:81], v[142:145], v[206:209], v[66:81]
	v_min3_f32 v210, v212, v90, v91
	v_and_or_b32 v95, v95, s1, 29
	v_med3_f32 v214, v210, v92, v93
	v_and_or_b32 v96, v96, s1, 30
	v_min3_f32 v212, v210, v92, v93
	v_and_or_b32 v97, v97, s1, 31
	v_min3_f32 v213, v213, v211, v214
	v_med3_f32 v211, v212, v94, v95
	v_min3_f32 v210, v212, v94, v95
	v_med3_f32 v214, v210, v96, v97
	v_min3_f32 v212, v210, v96, v97
	v_min3_f32 v213, v213, v211, v214
	v_mfma_f32_32x32x16_f16 v[82:97], v[146:149], v[194:197], v[50:65]
	v_and_or_b32 v66, v66, s1, 32
	v_and_or_b32 v67, v67, s1, 33
	v_and_or_b32 v68, v68, s1, 34
	v_and_or_b32 v69, v69, s1, 35
	v_med3_f32 v211, v212, v66, v67
	v_and_or_b32 v70, v70, s1, 36
	v_min3_f32 v210, v212, v66, v67
	v_and_or_b32 v71, v71, s1, 37
	v_mfma_f32_32x32x16_f16 v[82:97], v[150:153], v[198:201], v[82:97]
	v_med3_f32 v214, v210, v68, v69
	v_and_or_b32 v72, v72, s1, 38
	v_min3_f32 v212, v210, v68, v69
	v_and_or_b32 v73, v73, s1, 39
	v_min3_f32 v213, v213, v211, v214
	v_med3_f32 v211, v212, v70, v71
	v_and_or_b32 v74, v74, s1, 40
	v_min3_f32 v210, v212, v70, v71
	v_mfma_f32_32x32x16_f16 v[82:97], v[154:157], v[202:205], v[82:97]
	v_and_or_b32 v75, v75, s1, 41
	v_med3_f32 v214, v210, v72, v73
	v_and_or_b32 v76, v76, s1, 42
	v_min3_f32 v212, v210, v72, v73
	v_and_or_b32 v77, v77, s1, 43
	v_min3_f32 v213, v213, v211, v214
	v_med3_f32 v211, v212, v74, v75
	v_and_or_b32 v78, v78, s1, 44
	v_mfma_f32_32x32x16_f16 v[82:97], v[158:161], v[206:209], v[82:97]
	v_min3_f32 v210, v212, v74, v75
	v_and_or_b32 v79, v79, s1, 45
	v_med3_f32 v214, v210, v76, v77
	v_and_or_b32 v80, v80, s1, 46
	v_min3_f32 v212, v210, v76, v77
	v_and_or_b32 v81, v81, s1, 47
	v_min3_f32 v213, v213, v211, v214
	v_med3_f32 v211, v212, v78, v79
	v_min3_f32 v210, v212, v78, v79
	v_med3_f32 v214, v210, v80, v81
	v_min3_f32 v212, v210, v80, v81
	v_min3_f32 v213, v213, v211, v214
	v_and_or_b32 v82, v82, s1, 48
	v_and_or_b32 v83, v83, s1, 49
	v_and_or_b32 v84, v84, s1, 50
	v_and_or_b32 v85, v85, s1, 51
	v_med3_f32 v211, v212, v82, v83
	v_and_or_b32 v86, v86, s1, 52
	v_min3_f32 v210, v212, v82, v83
	v_and_or_b32 v87, v87, s1, 53
	v_med3_f32 v214, v210, v84, v85
	v_and_or_b32 v88, v88, s1, 54
	v_min3_f32 v212, v210, v84, v85
	v_and_or_b32 v89, v89, s1, 55
	v_min3_f32 v213, v213, v211, v214
	v_med3_f32 v211, v212, v86, v87
	v_and_or_b32 v90, v90, s1, 56
	v_min3_f32 v210, v212, v86, v87
	v_and_or_b32 v91, v91, s1, 57
	v_med3_f32 v214, v210, v88, v89
	v_and_or_b32 v92, v92, s1, 58
	v_min3_f32 v212, v210, v88, v89
	v_and_or_b32 v93, v93, s1, 59
	v_min3_f32 v213, v213, v211, v214
	v_med3_f32 v211, v212, v90, v91
	v_and_or_b32 v94, v94, s1, 60
	v_min3_f32 v210, v212, v90, v91
	v_and_or_b32 v95, v95, s1, 61
	v_med3_f32 v214, v210, v92, v93
	v_and_or_b32 v96, v96, s1, 62
	v_min3_f32 v212, v210, v92, v93
	v_or_b32_e32 v97, 63, v97
	v_min3_f32 v213, v213, v211, v214
	v_med3_f32 v211, v212, v94, v95
	v_min3_f32 v210, v212, v94, v95
	v_med3_f32 v214, v210, v96, v97
	v_min3_f32 v212, v210, v96, v97
	v_min3_f32 v213, v213, v211, v214
	ds_write_b64 v189, v[212:213]
	s_cmp_gt_u32 s5, 13
	s_cbranch_scc1 .Lld_even_noW
	s_and_b32 s6, s0, 2
	s_waitcnt vmcnt(3)
	v_cvt_pk_f16_f32 v67, v176, v177
	v_cvt_pk_f16_f32 v66, v174, v175
	s_lshl_b32 s6, s6, 13
	ds_write_b64 v192, v[66:67] offset:4608
	s_waitcnt vmcnt(2)
	v_cvt_pk_f16_f32 v67, v172, v173
	v_cvt_pk_f16_f32 v66, v170, v171
	s_or_b32 s6, s6, 0x12000
	ds_write_b64 v192, v[66:67] offset:6912
	v_lshl_or_b32 v66, v187, 4, s6
	ds_write_b128 v66, v[174:177]
	v_lshl_or_b32 v66, v188, 4, s6
	ds_write_b128 v66, v[170:173]
	s_min_u32 s6, s5, 11
	v_lshl_add_u32 v66, s6, 13, v191
	v_or_b32_e32 v66, v66, v178
	v_or_b32_e32 v67, 0x1000, v66
	global_load_dwordx4 v[174:177], v66, s[20:21] nt
	global_load_dwordx4 v[170:173], v67, s[20:21] nt
	s_waitcnt lgkmcnt(4)
	s_barrier
	s_branch .Lld_odd

.Lld_odd:
	ds_read_b128 v[194:197], v193 offset:4608
	ds_read_b128 v[198:201], v193 offset:4640
	ds_read_b128 v[202:205], v193 offset:4672
	ds_read_b128 v[206:209], v193 offset:4704
	s_add_i32 s0, s0, 2
	v_add_u32_e32 v192, 0x2400, v192
	v_add_u32_e32 v193, 0x2400, v193
	s_waitcnt lgkmcnt(3)
	v_mfma_f32_32x32x16_f16 v[66:81], v[98:101], v[194:197], v[2:17]
	s_waitcnt lgkmcnt(2)
	v_mfma_f32_32x32x16_f16 v[66:81], v[102:105], v[198:201], v[66:81]
	s_waitcnt lgkmcnt(1)
	v_mfma_f32_32x32x16_f16 v[66:81], v[106:109], v[202:205], v[66:81]
	s_waitcnt lgkmcnt(0)
	v_mfma_f32_32x32x16_f16 v[66:81], v[110:113], v[206:209], v[66:81]
	v_mfma_f32_32x32x16_f16 v[82:97], v[114:117], v[194:197], v[18:33]
	s_nop 10
	v_and_b32_e32 v66, 0xffffffc0, v66
	v_and_or_b32 v67, v67, s1, 1
	v_and_or_b32 v68, v68, s1, 2
	v_and_or_b32 v69, v69, s1, 3
	v_med3_f32 v211, v66, v67, s4
	v_and_or_b32 v70, v70, s1, 4
	v_min3_f32 v210, v66, s4, v67
	v_and_or_b32 v71, v71, s1, 5
	v_mfma_f32_32x32x16_f16 v[82:97], v[118:121], v[198:201], v[82:97]
	v_med3_f32 v214, v210, v68, v69
	v_and_or_b32 v72, v72, s1, 6
	v_min3_f32 v212, v210, v68, v69
	v_and_or_b32 v73, v73, s1, 7
	v_min3_f32 v213, v211, s4, v214
	v_med3_f32 v211, v212, v70, v71
	v_and_or_b32 v74, v74, s1, 8
	v_min3_f32 v210, v212, v70, v71
	v_mfma_f32_32x32x16_f16 v[82:97], v[122:125], v[202:205], v[82:97]
	v_and_or_b32 v75, v75, s1, 9
	v_med3_f32 v214, v210, v72, v73
	v_and_or_b32 v76, v76, s1, 10
	v_min3_f32 v212, v210, v72, v73
	v_and_or_b32 v77, v77, s1, 11
	v_min3_f32 v213, v213, v211, v214
	v_med3_f32 v211, v212, v74, v75
	v_and_or_b32 v78, v78, s1, 12
	v_mfma_f32_32x32x16_f16 v[82:97], v[126:129], v[206:209], v[82:97]
	v_min3_f32 v210, v212, v74, v75
	v_and_or_b32 v79, v79, s1, 13
	v_med3_f32 v214, v210, v76, v77
	v_and_or_b32 v80, v80, s1, 14
	v_min3_f32 v212, v210, v76, v77
	v_and_or_b32 v81, v81, s1, 15
	v_min3_f32 v213, v213, v211, v214
	v_med3_f32 v211, v212, v78, v79
	v_min3_f32 v210, v212, v78, v79
	v_med3_f32 v214, v210, v80, v81
	v_min3_f32 v212, v210, v80, v81
	v_min3_f32 v213, v213, v211, v214
	v_mfma_f32_32x32x16_f16 v[66:81], v[130:133], v[194:197], v[34:49]
	v_and_or_b32 v82, v82, s1, 16
	v_and_or_b32 v83, v83, s1, 17
	v_and_or_b32 v84, v84, s1, 18
	v_and_or_b32 v85, v85, s1, 19
	v_med3_f32 v211, v212, v82, v83
	v_and_or_b32 v86, v86, s1, 20
	v_min3_f32 v210, v212, v82, v83
	v_and_or_b32 v87, v87, s1, 21
	v_mfma_f32_32x32x16_f16 v[66:81], v[134:137], v[198:201], v[66:81]
	v_med3_f32 v214, v210, v84, v85
	v_and_or_b32 v88, v88, s1, 22
	v_min3_f32 v212, v210, v84, v85
	v_and_or_b32 v89, v89, s1, 23
	v_min3_f32 v213, v213, v211, v214
	v_med3_f32 v211, v212, v86, v87
	v_and_or_b32 v90, v90, s1, 24
	v_min3_f32 v210, v212, v86, v87
	v_mfma_f32_32x32x16_f16 v[66:81], v[138:141], v[202:205], v[66:81]
	v_and_or_b32 v91, v91, s1, 25
	v_med3_f32 v214, v210, v88, v89
	v_and_or_b32 v92, v92, s1, 26
	v_min3_f32 v212, v210, v88, v89
	v_and_or_b32 v93, v93, s1, 27
	v_min3_f32 v213, v213, v211, v214
	v_med3_f32 v211, v212, v90, v91
	v_and_or_b32 v94, v94, s1, 28
	v_mfma_f32_32x32x16_f16 v[66:81], v[142:145], v[206:209], v[66:81]
	v_min3_f32 v210, v212, v90, v91
	v_and_or_b32 v95, v95, s1, 29
	v_med3_f32 v214, v210, v92, v93
	v_and_or_b32 v96, v96, s1, 30
	v_min3_f32 v212, v210, v92, v93
	v_and_or_b32 v97, v97, s1, 31
	v_min3_f32 v213, v213, v211, v214
	v_med3_f32 v211, v212, v94, v95
	v_min3_f32 v210, v212, v94, v95
	v_med3_f32 v214, v210, v96, v97
	v_min3_f32 v212, v210, v96, v97
	v_min3_f32 v213, v213, v211, v214
	v_mfma_f32_32x32x16_f16 v[82:97], v[146:149], v[194:197], v[50:65]
	v_and_or_b32 v66, v66, s1, 32
	v_and_or_b32 v67, v67, s1, 33
	v_and_or_b32 v68, v68, s1, 34
	v_and_or_b32 v69, v69, s1, 35
	v_med3_f32 v211, v212, v66, v67
	v_and_or_b32 v70, v70, s1, 36
	v_min3_f32 v210, v212, v66, v67
	v_and_or_b32 v71, v71, s1, 37
	v_mfma_f32_32x32x16_f16 v[82:97], v[150:153], v[198:201], v[82:97]
	v_med3_f32 v214, v210, v68, v69
	v_and_or_b32 v72, v72, s1, 38
	v_min3_f32 v212, v210, v68, v69
	v_and_or_b32 v73, v73, s1, 39
	v_min3_f32 v213, v213, v211, v214
	v_med3_f32 v211, v212, v70, v71
	v_and_or_b32 v74, v74, s1, 40
	v_min3_f32 v210, v212, v70, v71
	v_mfma_f32_32x32x16_f16 v[82:97], v[154:157], v[202:205], v[82:97]
	v_and_or_b32 v75, v75, s1, 41
	v_med3_f32 v214, v210, v72, v73
	v_and_or_b32 v76, v76, s1, 42
	v_min3_f32 v212, v210, v72, v73
	v_and_or_b32 v77, v77, s1, 43
	v_min3_f32 v213, v213, v211, v214
	v_med3_f32 v211, v212, v74, v75
	v_and_or_b32 v78, v78, s1, 44
	v_mfma_f32_32x32x16_f16 v[82:97], v[158:161], v[206:209], v[82:97]
	v_min3_f32 v210, v212, v74, v75
	v_and_or_b32 v79, v79, s1, 45
	v_med3_f32 v214, v210, v76, v77
	v_and_or_b32 v80, v80, s1, 46
	v_min3_f32 v212, v210, v76, v77
	v_and_or_b32 v81, v81, s1, 47
	v_min3_f32 v213, v213, v211, v214
	v_med3_f32 v211, v212, v78, v79
	v_min3_f32 v210, v212, v78, v79
	v_med3_f32 v214, v210, v80, v81
	v_min3_f32 v212, v210, v80, v81
	v_min3_f32 v213, v213, v211, v214
	v_and_or_b32 v82, v82, s1, 48
	v_and_or_b32 v83, v83, s1, 49
	v_and_or_b32 v84, v84, s1, 50
	v_and_or_b32 v85, v85, s1, 51
	v_med3_f32 v211, v212, v82, v83
	v_and_or_b32 v86, v86, s1, 52
	v_min3_f32 v210, v212, v82, v83
	v_and_or_b32 v87, v87, s1, 53
	v_med3_f32 v214, v210, v84, v85
	v_and_or_b32 v88, v88, s1, 54
	v_min3_f32 v212, v210, v84, v85
	v_and_or_b32 v89, v89, s1, 55
	v_min3_f32 v213, v213, v211, v214
	v_med3_f32 v211, v212, v86, v87
	v_and_or_b32 v90, v90, s1, 56
	v_min3_f32 v210, v212, v86, v87
	v_and_or_b32 v91, v91, s1, 57
	v_med3_f32 v214, v210, v88, v89
	v_and_or_b32 v92, v92, s1, 58
	v_min3_f32 v212, v210, v88, v89
	v_and_or_b32 v93, v93, s1, 59
	v_min3_f32 v213, v213, v211, v214
	v_med3_f32 v211, v212, v90, v91
	v_and_or_b32 v94, v94, s1, 60
	v_min3_f32 v210, v212, v90, v91
	v_and_or_b32 v95, v95, s1, 61
	v_med3_f32 v214, v210, v92, v93
	v_and_or_b32 v96, v96, s1, 62
	v_min3_f32 v212, v210, v92, v93
	v_or_b32_e32 v97, 63, v97
	v_min3_f32 v213, v213, v211, v214
	v_med3_f32 v211, v212, v94, v95
	v_min3_f32 v210, v212, v94, v95
	v_med3_f32 v214, v210, v96, v97
	v_min3_f32 v212, v210, v96, v97
	v_min3_f32 v213, v213, v211, v214
	ds_write_b64 v189, v[212:213] offset:4608
	s_cmp_gt_u32 s5, 13
	s_cbranch_scc1 .Lld_exit
	s_waitcnt vmcnt(3)
	v_cvt_pk_f16_f32 v67, v168, v169
	v_cvt_pk_f16_f32 v66, v166, v167
	ds_write_b64 v192, v[66:67]
	s_waitcnt vmcnt(2)
	v_cvt_pk_f16_f32 v67, v164, v165
	v_cvt_pk_f16_f32 v66, v162, v163
	ds_write_b64 v192, v[66:67] offset:2304
	s_add_i32 s6, s0, -1
	s_add_i32 s5, s0, -2
	s_and_b32 s6, s6, 3
	s_min_u32 s7, s5, 12
	s_lshl_b32 s6, s6, 13
	v_lshl_add_u32 v66, s7, 13, v190
	s_add_i32 s6, s6, 0x12000
	v_or_b32_e32 v66, v66, v178
	v_lshl_or_b32 v67, v187, 4, s6
	v_lshl_or_b32 v84, v188, 4, s6
	v_or_b32_e32 v85, 0x1000, v66
	ds_write_b128 v67, v[166:169]
	ds_write_b128 v84, v[162:165]
	global_load_dwordx4 v[166:169], v66, s[20:21] nt
	global_load_dwordx4 v[162:165], v85, s[20:21] nt
	s_waitcnt lgkmcnt(4)
	s_barrier
	s_branch .Lld_even
.Lld_exit:
	s_waitcnt lgkmcnt(0)
	s_barrier
.LBB0_84:
	s_waitcnt lgkmcnt(0)
	s_barrier
	s_mov_b64 s[0:1], 0
